# same as previous plus has_next guard on the MoE-up token-list LDS-DMA (robustness)
# baseline (speedup 1.0000x reference)
; __device__ __forceinline__ int otid() { int t = threadIdx.x; asm volatile("" : "+v"(t)); return t; }
;     __device__ __forceinline__ bool next(int i, pg::Unit& u) const { u.aux = 0; u.aux2 = 0; u.half = 0; return ord.get(i, u.pm, u.pn); }
;     __device__ __forceinline__ bool next(int i, pg::Unit& u) const { u.aux = 0; u.aux2 = 0; u.half = 0; return ord.get(i, u.pm, u.pn); }
; template <class P, class MK = NoChain>
; __device__ __forceinline__ void gemm_phase(LAS unsigned char* lds, const P& p, const MK& mk = MK(), bool chain_out = false, bool chained_in = false) {
;     ...
;     for (;;) {
;         const bool has_next = p.next(ui + 1, nxt);
;         const char* nA = has_next ? p.a_base(nxt) : cA; const char* nB = has_next ? p.b_base(nxt) : cB;
;         const bool chain_now = CHAIN && chain_out && !has_next;
;         if constexpr (CHAIN) { if (chain_now) { const auto np = mk(); Unit nu; (void)np.next(0, nu); nA = np.a_base(nu); nB = np.b_base(nu); } }
;         const bool full = P::HALF ? (cur.half == 0) : true;
;     __device__ __forceinline__ void a_offsets(const pg::Unit& u, unsigned (&off)[2][2]) const {
;         int R[2], C[2]; { const int t_ = otid(); pg::stage_rc(t_ * 16, R[0], C[0]); pg::stage_rc(t_ * 16 + 8192, R[1], C[1]); }
;         if (u.aux < 64) {
;             const int n = T.cnt[u.aux]; const int* lp = LIST + (size_t)u.aux * NT + u.pm * 256;
; #pragma unroll
;             for (int h = 0; h < 2; ++h)
; #pragma unroll
;                 for (int i = 0; i < 2; ++i) { const int r = R[i] + 128 * h; const int tok = (u.pm * 256 + r < n) ? lp[r] : 0; off[h][i] = (unsigned)(tok * K + C[i] * 2); }
.LBB0_1490:
	s_cmp_gt_i32 s24, 63
	s_cselect_b64 s[0:1], -1, 0
	s_ashr_i32 s25, s24, 31
	s_lshl_b64 s[36:37], s[24:25], 15
	s_lshl_b32 s25, s24, 2
	s_add_i32 s25, s25, 0
	s_add_i32 s25, s25, 0x20100
	v_lshlrev_b32_e32 v194, 8, v237
	s_add_u32 s36, s49, s36
	v_ashrrev_i32_e32 v195, 31, v194
	s_addc_u32 s37, s50, s37
	v_lshlrev_b32_e32 v200, 19, v237
	s_waitcnt lgkmcnt(0)
	v_lshlrev_b64 v[2:3], 2, v[194:195]
	s_add_u32 s33, s34, 0x200
	v_or_b32_e32 v201, 0x40000, v200
	v_lshl_add_u64 v[196:197], s[36:37], 0, v[2:3]
	s_addc_u32 s70, s35, 0
	s_mov_b32 s71, 0
	s_mov_b64 s[34:35], s[20:21]
	s_andn2_b64 vcc, exec, s[30:31]
	s_cbranch_vccnz .Lg2_skip_a0
	v_and_b32_e32 v2, 63, v0
	v_lshlrev_b32_e32 v2, 4, v2
	v_mov_b32_e32 v3, 0
	v_lshl_add_u64 v[2:3], v[196:197], 0, v[2:3]
	v_readfirstlane_b32 s36, v0
	s_lshr_b32 s36, s36, 6
	s_lshl_b32 s36, s36, 10
	s_add_i32 s36, s36, 0x21000
	s_mov_b32 m0, s36
	s_nop 0
	global_load_lds_dwordx4 v[2:3], off
.Lg2_skip_a0:
	s_barrier
	s_branch .LBB0_1492
